# v28 + loop-edge edit of the phase-2/6 GEMM k-loops (stage offsets, m0 values, fragment addresses, tail/exit tests hoisted in front of the post-burst barrier; per-DMA m0 save/restore dropped)
# speedup vs baseline: 1.0273x; 1.0024x over previous
.LBB0_209:
	v_and_b32_e32 v14, 12, v10
	v_lshrrev_b32_e32 v12, 4, v10
	v_lshrrev_b32_e64 v14, v14, s57
	v_bfe_u32 v13, v10, 2, 2
	v_xor_b32_e32 v12, v14, v12
	v_lshrrev_b32_e32 v14, 2, v10
	s_lshl_b32 s8, s8, 5
	v_and_or_b32 v14, v14, 4, v13
	v_lshlrev_b32_e32 v15, 8, v10
	v_lshlrev_b32_e32 v13, 9, v13
	s_lshl_b32 s2, s2, 2
	v_and_b32_e32 v11, 15, v10
	s_and_b32 s8, s8, 0xffffe000
	v_lshlrev_b32_e32 v12, 4, v12
	v_bitop3_b32 v14, s2, v14, 12 bitop3:0x6c
	v_lshlrev_b32_e32 v10, 3, v10
	v_and_or_b32 v13, v15, s59, v13
	v_and_b32_e32 v10, 24, v10
	v_lshlrev_b32_e32 v11, 6, v11
	v_lshl_or_b32 v13, v14, 5, v13
	v_and_b32_e32 v12, 48, v12
	s_add_i32 s2, s8, 0
	v_lshl_add_u64 v[182:183], v[2:3], 0, s[46:47]
	v_mov_b32_e32 v2, 0
	s_mov_b32 s84, 2
	v_or_b32_e32 v178, v13, v10
	v_add3_u32 v188, s2, v11, v12
	v_bitop3_b32 v189, v13, 32, v10 bitop3:0x36
	v_bitop3_b32 v190, v13, 64, v10 bitop3:0x36
	v_bitop3_b32 v191, v13, s60, v10 bitop3:0x36
	v_lshl_add_u64 v[180:181], v[4:5], 0, s[46:47]
	v_lshl_add_u64 v[184:185], v[8:9], 0, s[54:55]
	v_lshl_add_u64 v[186:187], v[6:7], 0, s[54:55]
	s_mov_b32 s85, 0
	s_mov_b32 s86, 0
	v_mov_b32_e32 v3, v2
	v_mov_b32_e32 v4, v2
	v_mov_b32_e32 v5, v2
	v_mov_b32_e32 v6, v2
	v_mov_b32_e32 v7, v2
	v_mov_b32_e32 v8, v2
	v_mov_b32_e32 v9, v2
	v_mov_b32_e32 v14, v2
	v_mov_b32_e32 v15, v2
	v_mov_b32_e32 v16, v2
	v_mov_b32_e32 v17, v2
	v_mov_b32_e32 v10, v2
	v_mov_b32_e32 v11, v2
	v_mov_b32_e32 v12, v2
	v_mov_b32_e32 v13, v2
	v_mov_b32_e32 v18, v2
	v_mov_b32_e32 v19, v2
	v_mov_b32_e32 v20, v2
	v_mov_b32_e32 v21, v2
	v_mov_b32_e32 v22, v2
	v_mov_b32_e32 v23, v2
	v_mov_b32_e32 v24, v2
	v_mov_b32_e32 v25, v2
	v_mov_b32_e32 v30, v2
	v_mov_b32_e32 v31, v2
	v_mov_b32_e32 v32, v2
	v_mov_b32_e32 v33, v2
	v_mov_b32_e32 v26, v2
	v_mov_b32_e32 v27, v2
	v_mov_b32_e32 v28, v2
	v_mov_b32_e32 v29, v2
	v_mov_b32_e32 v34, v2
	v_mov_b32_e32 v35, v2
	v_mov_b32_e32 v36, v2
	v_mov_b32_e32 v37, v2
	v_mov_b32_e32 v38, v2
	v_mov_b32_e32 v39, v2
	v_mov_b32_e32 v40, v2
	v_mov_b32_e32 v41, v2
	v_mov_b32_e32 v50, v2
	v_mov_b32_e32 v51, v2
	v_mov_b32_e32 v52, v2
	v_mov_b32_e32 v53, v2
	v_mov_b32_e32 v42, v2
	v_mov_b32_e32 v43, v2
	v_mov_b32_e32 v44, v2
	v_mov_b32_e32 v45, v2
	v_mov_b32_e32 v46, v2
	v_mov_b32_e32 v47, v2
	v_mov_b32_e32 v48, v2
	v_mov_b32_e32 v49, v2
	v_mov_b32_e32 v54, v2
	v_mov_b32_e32 v55, v2
	v_mov_b32_e32 v56, v2
	v_mov_b32_e32 v57, v2
	v_mov_b32_e32 v66, v2
	v_mov_b32_e32 v67, v2
	v_mov_b32_e32 v68, v2
	v_mov_b32_e32 v69, v2
	v_mov_b32_e32 v58, v2
	v_mov_b32_e32 v59, v2
	v_mov_b32_e32 v60, v2
	v_mov_b32_e32 v61, v2
	v_mov_b32_e32 v62, v2
	v_mov_b32_e32 v63, v2
	v_mov_b32_e32 v64, v2
	v_mov_b32_e32 v65, v2
	v_mov_b32_e32 v70, v2
	v_mov_b32_e32 v71, v2
	v_mov_b32_e32 v72, v2
	v_mov_b32_e32 v73, v2
	v_mov_b32_e32 v86, v2
	v_mov_b32_e32 v87, v2
	v_mov_b32_e32 v88, v2
	v_mov_b32_e32 v89, v2
	v_mov_b32_e32 v74, v2
	v_mov_b32_e32 v75, v2
	v_mov_b32_e32 v76, v2
	v_mov_b32_e32 v77, v2
	v_mov_b32_e32 v78, v2
	v_mov_b32_e32 v79, v2
	v_mov_b32_e32 v80, v2
	v_mov_b32_e32 v81, v2
	v_mov_b32_e32 v82, v2
	v_mov_b32_e32 v83, v2
	v_mov_b32_e32 v84, v2
	v_mov_b32_e32 v85, v2
	v_mov_b32_e32 v102, v2
	v_mov_b32_e32 v103, v2
	v_mov_b32_e32 v104, v2
	v_mov_b32_e32 v105, v2
	v_mov_b32_e32 v90, v2
	v_mov_b32_e32 v91, v2
	v_mov_b32_e32 v92, v2
	v_mov_b32_e32 v93, v2
	v_mov_b32_e32 v94, v2
	v_mov_b32_e32 v95, v2
	v_mov_b32_e32 v96, v2
	v_mov_b32_e32 v97, v2
	v_mov_b32_e32 v98, v2
	v_mov_b32_e32 v99, v2
	v_mov_b32_e32 v100, v2
	v_mov_b32_e32 v101, v2
	v_mov_b32_e32 v118, v2
	v_mov_b32_e32 v119, v2
	v_mov_b32_e32 v120, v2
	v_mov_b32_e32 v121, v2
	v_mov_b32_e32 v106, v2
	v_mov_b32_e32 v107, v2
	v_mov_b32_e32 v108, v2
	v_mov_b32_e32 v109, v2
	v_mov_b32_e32 v110, v2
	v_mov_b32_e32 v111, v2
	v_mov_b32_e32 v112, v2
	v_mov_b32_e32 v113, v2
	v_mov_b32_e32 v114, v2
	v_mov_b32_e32 v115, v2
	v_mov_b32_e32 v116, v2
	v_mov_b32_e32 v117, v2
	v_mov_b32_e32 v126, v2
	v_mov_b32_e32 v127, v2
	v_mov_b32_e32 v128, v2
	v_mov_b32_e32 v129, v2
	v_mov_b32_e32 v122, v2
	v_mov_b32_e32 v123, v2
	v_mov_b32_e32 v124, v2
	v_mov_b32_e32 v125, v2
	s_lshl_b32 s2, s84, 14
	s_add_i32 s98, s2, s70
	s_add_i32 s99, s98, 0x2000
	s_add_i32 s100, s2, s71
	s_add_i32 s101, s100, 0x2000
	s_lshl_b32 s2, s86, 14
	v_add_u32_e32 v192, s2, v178
	v_add_u32_e32 v193, s2, v189
	v_add_u32_e32 v194, s2, v190
	v_add_u32_e32 v195, s2, v191
	v_add_u32_e32 v196, s2, v188
	s_cmp_gt_u32 s85, 61
	s_cselect_b64 vcc, exec, 0
	s_cmp_eq_u32 s85, 64
	s_mov_b32 s34, m0
	s_branch .LBB0_211
.LBB0_210:
	s_barrier
	s_waitcnt lgkmcnt(7)
	v_mfma_f32_16x16x32_bf16 v[122:125], v[130:133], v[174:177], v[122:125]
	v_mfma_f32_16x16x32_bf16 v[126:129], v[134:137], v[174:177], v[126:129]
	v_mfma_f32_16x16x32_bf16 v[114:117], v[138:141], v[174:177], v[114:117]
	v_mfma_f32_16x16x32_bf16 v[110:113], v[142:145], v[174:177], v[110:113]
	s_waitcnt lgkmcnt(6)
	v_mfma_f32_16x16x32_bf16 v[106:109], v[130:133], v[170:173], v[106:109]
	v_mfma_f32_16x16x32_bf16 v[118:121], v[134:137], v[170:173], v[118:121]
	v_mfma_f32_16x16x32_bf16 v[98:101], v[138:141], v[170:173], v[98:101]
	v_mfma_f32_16x16x32_bf16 v[94:97], v[142:145], v[170:173], v[94:97]
	s_waitcnt lgkmcnt(5)
	v_mfma_f32_16x16x32_bf16 v[90:93], v[130:133], v[166:169], v[90:93]
	v_mfma_f32_16x16x32_bf16 v[102:105], v[134:137], v[166:169], v[102:105]
	v_mfma_f32_16x16x32_bf16 v[82:85], v[138:141], v[166:169], v[82:85]
	v_mfma_f32_16x16x32_bf16 v[78:81], v[142:145], v[166:169], v[78:81]
	s_waitcnt lgkmcnt(4)
	v_mfma_f32_16x16x32_bf16 v[74:77], v[130:133], v[162:165], v[74:77]
	v_mfma_f32_16x16x32_bf16 v[86:89], v[134:137], v[162:165], v[86:89]
	v_mfma_f32_16x16x32_bf16 v[70:73], v[138:141], v[162:165], v[70:73]
	v_mfma_f32_16x16x32_bf16 v[62:65], v[142:145], v[162:165], v[62:65]
	s_waitcnt lgkmcnt(3)
	v_mfma_f32_16x16x32_bf16 v[58:61], v[130:133], v[158:161], v[58:61]
	v_mfma_f32_16x16x32_bf16 v[66:69], v[134:137], v[158:161], v[66:69]
	v_mfma_f32_16x16x32_bf16 v[54:57], v[138:141], v[158:161], v[54:57]
	v_mfma_f32_16x16x32_bf16 v[46:49], v[142:145], v[158:161], v[46:49]
	s_waitcnt lgkmcnt(2)
	v_mfma_f32_16x16x32_bf16 v[42:45], v[130:133], v[154:157], v[42:45]
	v_mfma_f32_16x16x32_bf16 v[50:53], v[134:137], v[154:157], v[50:53]
	v_mfma_f32_16x16x32_bf16 v[38:41], v[138:141], v[154:157], v[38:41]
	v_mfma_f32_16x16x32_bf16 v[34:37], v[142:145], v[154:157], v[34:37]
	s_waitcnt lgkmcnt(1)
	v_mfma_f32_16x16x32_bf16 v[26:29], v[130:133], v[150:153], v[26:29]
	v_mfma_f32_16x16x32_bf16 v[30:33], v[134:137], v[150:153], v[30:33]
	v_mfma_f32_16x16x32_bf16 v[22:25], v[138:141], v[150:153], v[22:25]
	v_mfma_f32_16x16x32_bf16 v[18:21], v[142:145], v[150:153], v[18:21]
	s_waitcnt lgkmcnt(0)
	v_mfma_f32_16x16x32_bf16 v[10:13], v[130:133], v[146:149], v[10:13]
	v_mfma_f32_16x16x32_bf16 v[14:17], v[134:137], v[146:149], v[14:17]
	v_mfma_f32_16x16x32_bf16 v[6:9], v[138:141], v[146:149], v[6:9]
	v_mfma_f32_16x16x32_bf16 v[2:5], v[142:145], v[146:149], v[2:5]
	s_add_i32 s2, s86, 1
	s_cmp_lg_u32 s86, 2
	s_cselect_b32 s86, s2, 0
	s_add_i32 s2, s84, 1
	s_cmp_lg_u32 s84, 2
	s_cselect_b32 s84, s2, 0
	s_add_i32 s85, s85, 1
	v_lshl_add_u64 v[180:181], v[180:181], 0, 64
	v_lshl_add_u64 v[182:183], v[182:183], 0, 64
	v_lshl_add_u64 v[184:185], v[184:185], 0, s[40:41]
	v_lshl_add_u64 v[186:187], v[186:187], 0, s[40:41]
	s_lshl_b32 s2, s84, 14
	s_add_i32 s98, s2, s70
	s_add_i32 s99, s98, 0x2000
	s_add_i32 s100, s2, s71
	s_add_i32 s101, s100, 0x2000
	s_lshl_b32 s2, s86, 14
	v_add_u32_e32 v192, s2, v178
	v_add_u32_e32 v193, s2, v189
	v_add_u32_e32 v194, s2, v190
	v_add_u32_e32 v195, s2, v191
	v_add_u32_e32 v196, s2, v188
	s_cmp_gt_u32 s85, 61
	s_cselect_b64 vcc, exec, 0
	s_cmp_eq_u32 s85, 64
	s_barrier
	s_cbranch_scc1 .Lp2_exit
.LBB0_211:
	s_cbranch_vccnz .Lp2_nodma
	s_mov_b32 m0, s98
	s_nop 0
	global_load_lds_dwordx4 v[182:183], off
	s_mov_b32 m0, s99
	s_nop 0
	global_load_lds_dwordx4 v[180:181], off
	s_mov_b32 m0, s100
	s_nop 0
	global_load_lds_dwordx4 v[186:187], off
	s_mov_b32 m0, s101
	s_nop 0
	global_load_lds_dwordx4 v[184:185], off
.Lp2_nodma:
	ds_read_b64_tr_b16 v[130:131], v192 offset:49152
	ds_read_b64_tr_b16 v[132:133], v192 offset:51200
	ds_read_b64_tr_b16 v[134:135], v193 offset:49152
	ds_read_b64_tr_b16 v[136:137], v193 offset:51200
	ds_read_b64_tr_b16 v[138:139], v194 offset:49152
	ds_read_b64_tr_b16 v[140:141], v194 offset:51200
	ds_read_b64_tr_b16 v[142:143], v195 offset:49152
	ds_read_b64_tr_b16 v[144:145], v195 offset:51200
	ds_read_b128 v[174:177], v196
	ds_read_b128 v[170:173], v196 offset:1024
	ds_read_b128 v[166:169], v196 offset:2048
	ds_read_b128 v[162:165], v196 offset:3072
	ds_read_b128 v[158:161], v196 offset:4096
	ds_read_b128 v[154:157], v196 offset:5120
	ds_read_b128 v[150:153], v196 offset:6144
	ds_read_b128 v[146:149], v196 offset:7168
	s_cbranch_vccnz .Lp2_tail
	s_waitcnt vmcnt(4) lgkmcnt(0)
	s_branch .LBB0_210
.Lp2_tail:
	s_waitcnt vmcnt(0) lgkmcnt(0)
	s_branch .LBB0_210
.Lp2_exit:
	s_mov_b32 m0, s34

.LBB0_613:
	v_and_b32_e32 v13, 12, v10
	v_lshrrev_b32_e32 v11, 4, v10
	v_lshrrev_b32_e64 v13, v13, s46
	v_bfe_u32 v12, v10, 2, 2
	v_xor_b32_e32 v11, v13, v11
	v_lshrrev_b32_e32 v13, 2, v10
	s_lshl_b32 s33, s33, 5
	v_and_or_b32 v13, v13, 4, v12
	v_lshlrev_b32_e32 v14, 8, v10
	v_lshlrev_b32_e32 v12, 9, v12
	s_lshl_b32 s2, s2, 2
	v_and_b32_e32 v1, 15, v10
	s_and_b32 s33, s33, 0xffffe000
	v_lshlrev_b32_e32 v11, 4, v11
	v_bitop3_b32 v13, s2, v13, 12 bitop3:0x6c
	v_lshlrev_b32_e32 v10, 3, v10
	v_and_or_b32 v12, v14, s47, v12
	v_and_b32_e32 v10, 24, v10
	v_lshlrev_b32_e32 v1, 6, v1
	v_lshl_or_b32 v12, v13, 5, v12
	v_and_b32_e32 v11, 48, v11
	s_add_i32 s2, s33, 0
	v_lshl_add_u64 v[182:183], v[2:3], 0, s[24:25]
	v_mov_b32_e32 v2, 0
	s_mov_b32 s60, 2
	v_or_b32_e32 v178, v12, v10
	v_add3_u32 v188, s2, v1, v11
	v_bitop3_b32 v189, v12, 32, v10 bitop3:0x36
	v_bitop3_b32 v190, v12, 64, v10 bitop3:0x36
	v_bitop3_b32 v191, v12, s54, v10 bitop3:0x36
	v_lshl_add_u64 v[180:181], v[4:5], 0, s[24:25]
	v_lshl_add_u64 v[184:185], v[8:9], 0, s[26:27]
	v_lshl_add_u64 v[186:187], v[6:7], 0, s[26:27]
	s_mov_b32 s61, 0
	s_mov_b32 s62, 0
	v_mov_b32_e32 v3, v2
	v_mov_b32_e32 v4, v2
	v_mov_b32_e32 v5, v2
	v_mov_b32_e32 v26, v2
	v_mov_b32_e32 v27, v2
	v_mov_b32_e32 v28, v2
	v_mov_b32_e32 v29, v2
	v_mov_b32_e32 v58, v2
	v_mov_b32_e32 v59, v2
	v_mov_b32_e32 v60, v2
	v_mov_b32_e32 v61, v2
	v_mov_b32_e32 v90, v2
	v_mov_b32_e32 v91, v2
	v_mov_b32_e32 v92, v2
	v_mov_b32_e32 v93, v2
	v_mov_b32_e32 v6, v2
	v_mov_b32_e32 v7, v2
	v_mov_b32_e32 v8, v2
	v_mov_b32_e32 v9, v2
	v_mov_b32_e32 v34, v2
	v_mov_b32_e32 v35, v2
	v_mov_b32_e32 v36, v2
	v_mov_b32_e32 v37, v2
	v_mov_b32_e32 v66, v2
	v_mov_b32_e32 v67, v2
	v_mov_b32_e32 v68, v2
	v_mov_b32_e32 v69, v2
	v_mov_b32_e32 v98, v2
	v_mov_b32_e32 v99, v2
	v_mov_b32_e32 v100, v2
	v_mov_b32_e32 v101, v2
	v_mov_b32_e32 v10, v2
	v_mov_b32_e32 v11, v2
	v_mov_b32_e32 v12, v2
	v_mov_b32_e32 v13, v2
	v_mov_b32_e32 v42, v2
	v_mov_b32_e32 v43, v2
	v_mov_b32_e32 v44, v2
	v_mov_b32_e32 v45, v2
	v_mov_b32_e32 v74, v2
	v_mov_b32_e32 v75, v2
	v_mov_b32_e32 v76, v2
	v_mov_b32_e32 v77, v2
	v_mov_b32_e32 v106, v2
	v_mov_b32_e32 v107, v2
	v_mov_b32_e32 v108, v2
	v_mov_b32_e32 v109, v2
	v_mov_b32_e32 v14, v2
	v_mov_b32_e32 v15, v2
	v_mov_b32_e32 v16, v2
	v_mov_b32_e32 v17, v2
	v_mov_b32_e32 v46, v2
	v_mov_b32_e32 v47, v2
	v_mov_b32_e32 v48, v2
	v_mov_b32_e32 v49, v2
	v_mov_b32_e32 v78, v2
	v_mov_b32_e32 v79, v2
	v_mov_b32_e32 v80, v2
	v_mov_b32_e32 v81, v2
	v_mov_b32_e32 v110, v2
	v_mov_b32_e32 v111, v2
	v_mov_b32_e32 v112, v2
	v_mov_b32_e32 v113, v2
	v_mov_b32_e32 v18, v2
	v_mov_b32_e32 v19, v2
	v_mov_b32_e32 v20, v2
	v_mov_b32_e32 v21, v2
	v_mov_b32_e32 v50, v2
	v_mov_b32_e32 v51, v2
	v_mov_b32_e32 v52, v2
	v_mov_b32_e32 v53, v2
	v_mov_b32_e32 v82, v2
	v_mov_b32_e32 v83, v2
	v_mov_b32_e32 v84, v2
	v_mov_b32_e32 v85, v2
	v_mov_b32_e32 v114, v2
	v_mov_b32_e32 v115, v2
	v_mov_b32_e32 v116, v2
	v_mov_b32_e32 v117, v2
	v_mov_b32_e32 v22, v2
	v_mov_b32_e32 v23, v2
	v_mov_b32_e32 v24, v2
	v_mov_b32_e32 v25, v2
	v_mov_b32_e32 v54, v2
	v_mov_b32_e32 v55, v2
	v_mov_b32_e32 v56, v2
	v_mov_b32_e32 v57, v2
	v_mov_b32_e32 v86, v2
	v_mov_b32_e32 v87, v2
	v_mov_b32_e32 v88, v2
	v_mov_b32_e32 v89, v2
	v_mov_b32_e32 v118, v2
	v_mov_b32_e32 v119, v2
	v_mov_b32_e32 v120, v2
	v_mov_b32_e32 v121, v2
	v_mov_b32_e32 v30, v2
	v_mov_b32_e32 v31, v2
	v_mov_b32_e32 v32, v2
	v_mov_b32_e32 v33, v2
	v_mov_b32_e32 v62, v2
	v_mov_b32_e32 v63, v2
	v_mov_b32_e32 v64, v2
	v_mov_b32_e32 v65, v2
	v_mov_b32_e32 v94, v2
	v_mov_b32_e32 v95, v2
	v_mov_b32_e32 v96, v2
	v_mov_b32_e32 v97, v2
	v_mov_b32_e32 v122, v2
	v_mov_b32_e32 v123, v2
	v_mov_b32_e32 v124, v2
	v_mov_b32_e32 v125, v2
	v_mov_b32_e32 v38, v2
	v_mov_b32_e32 v39, v2
	v_mov_b32_e32 v40, v2
	v_mov_b32_e32 v41, v2
	v_mov_b32_e32 v70, v2
	v_mov_b32_e32 v71, v2
	v_mov_b32_e32 v72, v2
	v_mov_b32_e32 v73, v2
	v_mov_b32_e32 v102, v2
	v_mov_b32_e32 v103, v2
	v_mov_b32_e32 v104, v2
	v_mov_b32_e32 v105, v2
	v_mov_b32_e32 v126, v2
	v_mov_b32_e32 v127, v2
	v_mov_b32_e32 v128, v2
	v_mov_b32_e32 v129, v2
	s_lshl_b32 s2, s60, 14
	s_add_i32 s98, s2, s58
	s_add_i32 s99, s98, 0x2000
	s_add_i32 s100, s2, s59
	s_add_i32 s101, s100, 0x2000
	s_lshl_b32 s2, s62, 14
	v_add_u32_e32 v192, s2, v178
	v_add_u32_e32 v193, s2, v189
	v_add_u32_e32 v194, s2, v190
	v_add_u32_e32 v195, s2, v191
	v_add_u32_e32 v196, s2, v188
	s_cmp_gt_u32 s61, 61
	s_cselect_b64 vcc, exec, 0
	s_cmp_eq_u32 s61, 64
	s_mov_b32 s40, m0
	s_branch .LBB0_615
.LBB0_614:
	s_barrier
	s_waitcnt lgkmcnt(7)
	v_mfma_f32_16x16x32_bf16 v[126:129], v[130:133], v[174:177], v[126:129]
	v_mfma_f32_16x16x32_bf16 v[102:105], v[134:137], v[174:177], v[102:105]
	v_mfma_f32_16x16x32_bf16 v[70:73], v[138:141], v[174:177], v[70:73]
	v_mfma_f32_16x16x32_bf16 v[38:41], v[142:145], v[174:177], v[38:41]
	s_waitcnt lgkmcnt(6)
	v_mfma_f32_16x16x32_bf16 v[122:125], v[130:133], v[170:173], v[122:125]
	v_mfma_f32_16x16x32_bf16 v[94:97], v[134:137], v[170:173], v[94:97]
	v_mfma_f32_16x16x32_bf16 v[62:65], v[138:141], v[170:173], v[62:65]
	v_mfma_f32_16x16x32_bf16 v[30:33], v[142:145], v[170:173], v[30:33]
	s_waitcnt lgkmcnt(5)
	v_mfma_f32_16x16x32_bf16 v[118:121], v[130:133], v[166:169], v[118:121]
	v_mfma_f32_16x16x32_bf16 v[86:89], v[134:137], v[166:169], v[86:89]
	v_mfma_f32_16x16x32_bf16 v[54:57], v[138:141], v[166:169], v[54:57]
	v_mfma_f32_16x16x32_bf16 v[22:25], v[142:145], v[166:169], v[22:25]
	s_waitcnt lgkmcnt(4)
	v_mfma_f32_16x16x32_bf16 v[114:117], v[130:133], v[162:165], v[114:117]
	v_mfma_f32_16x16x32_bf16 v[82:85], v[134:137], v[162:165], v[82:85]
	v_mfma_f32_16x16x32_bf16 v[50:53], v[138:141], v[162:165], v[50:53]
	v_mfma_f32_16x16x32_bf16 v[18:21], v[142:145], v[162:165], v[18:21]
	s_waitcnt lgkmcnt(3)
	v_mfma_f32_16x16x32_bf16 v[110:113], v[130:133], v[158:161], v[110:113]
	v_mfma_f32_16x16x32_bf16 v[78:81], v[134:137], v[158:161], v[78:81]
	v_mfma_f32_16x16x32_bf16 v[46:49], v[138:141], v[158:161], v[46:49]
	v_mfma_f32_16x16x32_bf16 v[14:17], v[142:145], v[158:161], v[14:17]
	s_waitcnt lgkmcnt(2)
	v_mfma_f32_16x16x32_bf16 v[106:109], v[130:133], v[154:157], v[106:109]
	v_mfma_f32_16x16x32_bf16 v[74:77], v[134:137], v[154:157], v[74:77]
	v_mfma_f32_16x16x32_bf16 v[42:45], v[138:141], v[154:157], v[42:45]
	v_mfma_f32_16x16x32_bf16 v[10:13], v[142:145], v[154:157], v[10:13]
	s_waitcnt lgkmcnt(1)
	v_mfma_f32_16x16x32_bf16 v[98:101], v[130:133], v[150:153], v[98:101]
	v_mfma_f32_16x16x32_bf16 v[66:69], v[134:137], v[150:153], v[66:69]
	v_mfma_f32_16x16x32_bf16 v[34:37], v[138:141], v[150:153], v[34:37]
	v_mfma_f32_16x16x32_bf16 v[6:9], v[142:145], v[150:153], v[6:9]
	s_waitcnt lgkmcnt(0)
	v_mfma_f32_16x16x32_bf16 v[90:93], v[130:133], v[146:149], v[90:93]
	v_mfma_f32_16x16x32_bf16 v[58:61], v[134:137], v[146:149], v[58:61]
	v_mfma_f32_16x16x32_bf16 v[26:29], v[138:141], v[146:149], v[26:29]
	v_mfma_f32_16x16x32_bf16 v[2:5], v[142:145], v[146:149], v[2:5]
	s_add_i32 s2, s62, 1
	s_cmp_lg_u32 s62, 2
	s_cselect_b32 s62, s2, 0
	s_add_i32 s2, s60, 1
	s_cmp_lg_u32 s60, 2
	s_cselect_b32 s60, s2, 0
	s_add_i32 s61, s61, 1
	v_lshl_add_u64 v[180:181], v[180:181], 0, 64
	v_lshl_add_u64 v[182:183], v[182:183], 0, 64
	v_lshl_add_u64 v[184:185], v[184:185], 0, s[20:21]
	v_lshl_add_u64 v[186:187], v[186:187], 0, s[20:21]
	s_lshl_b32 s2, s60, 14
	s_add_i32 s98, s2, s58
	s_add_i32 s99, s98, 0x2000
	s_add_i32 s100, s2, s59
	s_add_i32 s101, s100, 0x2000
	s_lshl_b32 s2, s62, 14
	v_add_u32_e32 v192, s2, v178
	v_add_u32_e32 v193, s2, v189
	v_add_u32_e32 v194, s2, v190
	v_add_u32_e32 v195, s2, v191
	v_add_u32_e32 v196, s2, v188
	s_cmp_gt_u32 s61, 61
	s_cselect_b64 vcc, exec, 0
	s_cmp_eq_u32 s61, 64
	s_barrier
	s_cbranch_scc1 .Lp6_exit

.Lp6_exit:
	s_mov_b32 m0, s40
